# speedup vs baseline: 1.0116x; 1.0007x over previous
.LBB1_117:
	s_andn2_b64 vcc, exec, s[20:21]
	s_cbranch_vccnz .LBB1_126
	s_setprio 3
	s_waitcnt lgkmcnt(0)
	s_load_dwordx4 s[8:11], s[0:1], 0x0
	s_bfe_u32 s4, s2, 0x20005
	s_lshl_b32 s0, s2, 6
	v_and_b32_e32 v10, 63, v0
	s_and_b32 s3, s0, 0x7c0
	s_mul_i32 s7, s4, 0x6000
	s_waitcnt lgkmcnt(0)
	s_add_u32 s0, s8, s7
	v_or_b32_e32 v1, s3, v10
	s_addc_u32 s1, s9, 0
	v_lshlrev_b32_e32 v2, 2, v1
	v_mov_b32_e32 v3, 0
	v_lshl_add_u64 v[4:5], s[0:1], 0, v[2:3]
	s_movk_i32 s5, 0x2000
	v_add_co_u32_e32 v6, vcc, s5, v4
	s_movk_i32 s5, 0x4000
	s_nop 0
	v_addc_co_u32_e32 v7, vcc, 0, v5, vcc
	v_add_co_u32_e32 v4, vcc, s5, v4
	v_readfirstlane_b32 s5, v0
	s_nop 0
	v_addc_co_u32_e32 v5, vcc, 0, v5, vcc
	global_load_dword v11, v2, s[0:1]
	global_load_dword v12, v[6:7], off
	global_load_dword v13, v[4:5], off
	s_lshr_b32 s6, s5, 6
	s_cmpk_lt_u32 s2, 0x80
	s_cselect_b32 s8, s8, s10
	s_cselect_b32 s0, s9, s11
	s_add_u32 s7, s8, s7
	s_mov_b32 s1, 0
	s_addc_u32 s8, s0, 0
	s_lshl_b32 s0, s6, 8
	s_lshl_b64 s[0:1], s[0:1], 2
	s_add_u32 s7, s7, s0
	s_addc_u32 s8, s8, s1
	v_mov_b32_e32 v9, 0x7f800000
	s_mov_b64 s[0:1], 0
	v_mov_b32_e32 v14, 0x2000
	v_mov_b32_e32 v15, 0x4000
	v_mov_b32_e32 v8, 0x7f800000
	v_mov_b32_e32 v7, 0x7f800000
	v_mov_b32_e32 v6, 0x7f800000
	v_mov_b32_e32 v5, 0x7f800000
	v_mov_b32_e32 v4, 0x7f800000
	v_mov_b32_e32 v2, 0x7f800000
	v_mov_b32_e32 v1, 0x7f800000
	s_mov_b32 s10, s7
	s_mov_b32 s11, s8
	s_load_dwordx8 s[20:27], s[10:11], 0x0
	s_load_dwordx8 s[28:35], s[10:11], 0x2000
	s_load_dwordx8 s[36:43], s[10:11], 0x4000
	s_mov_b32 s0, 0
	s_waitcnt vmcnt(0) lgkmcnt(0)
